# P8 and P9 expert GEMM epilogues: lanes regrouped with ds_bpermute so each quad stores 32 contiguous bytes of one row (no LDS staging)
# baseline (speedup 1.0000x reference)
.LBB0_899:
	s_lshl_b32 s3, s42, 7
	s_and_b32 s3, s3, 0x380
	v_or_b32_e32 v2, s3, v213
	s_lshl_b32 s74, s69, 18
	s_add_i32 s74, s74, s3
	s_add_u32 s74, s14, s74
	s_addc_u32 s75, s15, 0
	s_add_u32 s46, s74, 0x2c000
	s_addc_u32 s47, s75, 0
	s_lshl_b32 s3, s68, 10
	s_and_b32 s3, s3, 0x400
	s_nop 15
	s_nop 15
	v_add_u32_e32 v4, s3, v209
	ds_read_b128 v[16:19], v4
	ds_read_b128 v[12:15], v4 offset:16
	ds_read_b128 v[8:11], v4 offset:512
	ds_read_b128 v[4:7], v4 offset:528
	v_and_b32_e32 v53, 63, v0
	v_and_b32_e32 v54, 3, v53
	v_lshrrev_b32_e32 v55, 2, v53
	v_lshl_or_b32 v46, v54, 4, v55
	v_lshlrev_b32_e32 v46, 2, v46
	v_and_b32_e32 v53, 0xfffffff0, v225
	v_or_b32_e32 v53, v53, v55
	v_and_b32_e32 v55, 0xffffffe7, v213
	v_lshl_or_b32 v55, v54, 3, v55
	v_lshl_or_b32 v52, v53, 10, v55
	v_lshl_add_u32 v24, s69, 8, v225
	s_waitcnt lgkmcnt(0)
	v_pk_add_f32 v[20:21], v[82:83], v[18:19]
	v_pk_add_f32 v[26:27], v[80:81], v[16:17]
	v_pk_add_f32 v[34:35], v[144:145], v[8:9]
	v_min_f32_e32 v26, 0x40e00000, v26
	v_min_f32_e32 v27, 0x40e00000, v27
	v_med3_f32 v34, v34, s30, v252
	v_med3_f32 v35, v35, s30, v252
	v_min_f32_e32 v20, 0x40e00000, v20
	v_min_f32_e32 v21, 0x40e00000, v21
	v_pk_mul_f32 v[38:39], v[26:27], s[86:87] op_sel_hi:[1,0]
	v_pk_fma_f32 v[26:27], v[26:27], v[34:35], v[26:27]
	v_pk_mul_f32 v[34:35], v[20:21], s[86:87] op_sel_hi:[1,0]
	v_pk_add_f32 v[30:31], v[88:89], v[12:13]
	v_exp_f32_e32 v34, v34
	v_exp_f32_e32 v35, v35
	v_pk_add_f32 v[32:33], v[146:147], v[10:11]
	v_min_f32_e32 v30, 0x40e00000, v30
	v_med3_f32 v32, v32, s30, v252
	v_pk_add_f32 v[34:35], v[34:35], 1.0 op_sel_hi:[1,0]
	v_med3_f32 v33, v33, s30, v252
	v_rcp_f32_e32 v34, v34
	v_rcp_f32_e32 v35, v35
	v_min_f32_e32 v31, 0x40e00000, v31
	v_pk_fma_f32 v[20:21], v[20:21], v[32:33], v[20:21]
	v_pk_mul_f32 v[32:33], v[30:31], s[86:87] op_sel_hi:[1,0]
	v_exp_f32_e32 v38, v38
	v_exp_f32_e32 v39, v39
	v_exp_f32_e32 v32, v32
	v_exp_f32_e32 v33, v33
	v_pk_add_f32 v[28:29], v[90:91], v[14:15]
	v_pk_add_f32 v[40:41], v[154:155], v[4:5]
	v_pk_mul_f32 v[20:21], v[20:21], v[34:35]
	v_med3_f32 v34, v40, s30, v252
	v_med3_f32 v35, v41, s30, v252
	v_min_f32_e32 v28, 0x40e00000, v28
	v_min_f32_e32 v29, 0x40e00000, v29
	v_pk_fma_f32 v[30:31], v[30:31], v[34:35], v[30:31]
	v_pk_mul_f32 v[34:35], v[28:29], s[86:87] op_sel_hi:[1,0]
	v_pk_add_f32 v[38:39], v[38:39], 1.0 op_sel_hi:[1,0]
	v_pk_add_f32 v[32:33], v[32:33], 1.0 op_sel_hi:[1,0]
	v_exp_f32_e32 v34, v34
	v_exp_f32_e32 v35, v35
	v_rcp_f32_e32 v38, v38
	v_rcp_f32_e32 v39, v39
	v_rcp_f32_e32 v32, v32
	v_rcp_f32_e32 v33, v33
	v_pk_add_f32 v[36:37], v[156:157], v[6:7]
	v_pk_add_f32 v[34:35], v[34:35], 1.0 op_sel_hi:[1,0]
	v_pk_mul_f32 v[26:27], v[26:27], v[38:39]
	v_pk_mul_f32 v[30:31], v[30:31], v[32:33]
	v_med3_f32 v32, v36, s30, v252
	v_med3_f32 v33, v37, s30, v252
	v_rcp_f32_e32 v34, v34
	v_rcp_f32_e32 v35, v35
	v_mov_b32_e32 v36, v3
	v_mov_b32_e32 v37, v3
	v_cvt_pk_fp8_f32 v36, v26, v27
	v_cvt_pk_fp8_f32 v37, v30, v31
	v_pk_fma_f32 v[26:27], v[28:29], v[32:33], v[28:29]
	v_pk_add_f32 v[28:29], v[98:99], v[18:19]
	v_pk_add_f32 v[30:31], v[96:97], v[16:17]
	v_pk_add_f32 v[38:39], v[158:159], v[8:9]
	v_min_f32_e32 v30, 0x40e00000, v30
	v_min_f32_e32 v31, 0x40e00000, v31
	v_med3_f32 v38, v38, s30, v252
	v_med3_f32 v39, v39, s30, v252
	v_min_f32_e32 v28, 0x40e00000, v28
	v_min_f32_e32 v29, 0x40e00000, v29
	v_pk_mul_f32 v[26:27], v[26:27], v[34:35]
	v_pk_mul_f32 v[42:43], v[30:31], s[86:87] op_sel_hi:[1,0]
	v_pk_fma_f32 v[30:31], v[30:31], v[38:39], v[30:31]
	v_pk_mul_f32 v[38:39], v[28:29], s[86:87] op_sel_hi:[1,0]
	v_cvt_pk_fp8_f32 v36, v20, v21 op_sel:[0,0,1]
	v_cvt_pk_fp8_f32 v37, v26, v27 op_sel:[0,0,1]
	v_exp_f32_e32 v38, v38
	v_exp_f32_e32 v39, v39
	v_ashrrev_i32_e32 v25, 31, v24
	v_lshl_add_u64 v[22:23], s[14:15], 0, v[2:3]
	v_lshlrev_b64 v[20:21], 10, v[24:25]
	v_lshl_add_u64 v[20:21], v[22:23], 0, v[20:21]
	ds_bpermute_b32 v48, v46, v36
	ds_bpermute_b32 v49, v46, v37
	v_pk_add_f32 v[34:35], v[104:105], v[12:13]
	v_pk_add_f32 v[36:37], v[160:161], v[10:11]
	v_pk_add_f32 v[38:39], v[38:39], 1.0 op_sel_hi:[1,0]
	v_med3_f32 v36, v36, s30, v252
	v_med3_f32 v37, v37, s30, v252
	v_rcp_f32_e32 v38, v38
	v_rcp_f32_e32 v39, v39
	v_min_f32_e32 v34, 0x40e00000, v34
	v_min_f32_e32 v35, 0x40e00000, v35
	v_pk_fma_f32 v[28:29], v[28:29], v[36:37], v[28:29]
	v_pk_mul_f32 v[36:37], v[34:35], s[86:87] op_sel_hi:[1,0]
	v_exp_f32_e32 v42, v42
	v_exp_f32_e32 v43, v43
	v_exp_f32_e32 v36, v36
	v_exp_f32_e32 v37, v37
	v_pk_add_f32 v[32:33], v[106:107], v[14:15]
	v_pk_add_f32 v[44:45], v[162:163], v[4:5]
	v_pk_mul_f32 v[28:29], v[28:29], v[38:39]
	v_med3_f32 v38, v44, s30, v252
	v_med3_f32 v39, v45, s30, v252
	v_min_f32_e32 v32, 0x40e00000, v32
	v_min_f32_e32 v33, 0x40e00000, v33
	v_pk_fma_f32 v[34:35], v[34:35], v[38:39], v[34:35]
	v_pk_mul_f32 v[38:39], v[32:33], s[86:87] op_sel_hi:[1,0]
	v_pk_add_f32 v[42:43], v[42:43], 1.0 op_sel_hi:[1,0]
	v_pk_add_f32 v[36:37], v[36:37], 1.0 op_sel_hi:[1,0]
	v_exp_f32_e32 v38, v38
	v_exp_f32_e32 v39, v39
	v_rcp_f32_e32 v42, v42
	v_rcp_f32_e32 v43, v43
	v_rcp_f32_e32 v36, v36
	v_rcp_f32_e32 v37, v37
	v_pk_add_f32 v[40:41], v[164:165], v[6:7]
	v_pk_add_f32 v[38:39], v[38:39], 1.0 op_sel_hi:[1,0]
	v_pk_mul_f32 v[30:31], v[30:31], v[42:43]
	v_pk_mul_f32 v[34:35], v[34:35], v[36:37]
	v_med3_f32 v36, v40, s30, v252
	v_med3_f32 v37, v41, s30, v252
	v_rcp_f32_e32 v38, v38
	v_rcp_f32_e32 v39, v39
	v_mov_b32_e32 v40, v3
	v_mov_b32_e32 v41, v3
	v_cvt_pk_fp8_f32 v40, v30, v31
	v_cvt_pk_fp8_f32 v41, v34, v35
	v_pk_fma_f32 v[30:31], v[32:33], v[36:37], v[32:33]
	v_pk_add_f32 v[34:35], v[120:121], v[12:13]
	v_pk_mul_f32 v[30:31], v[30:31], v[38:39]
	v_cvt_pk_fp8_f32 v40, v28, v29 op_sel:[0,0,1]
	v_cvt_pk_fp8_f32 v41, v30, v31 op_sel:[0,0,1]
	v_pk_add_f32 v[28:29], v[114:115], v[18:19]
	v_pk_add_f32 v[30:31], v[112:113], v[16:17]
	v_pk_add_f32 v[38:39], v[166:167], v[8:9]
	v_min_f32_e32 v30, 0x40e00000, v30
	v_min_f32_e32 v31, 0x40e00000, v31
	v_med3_f32 v38, v38, s30, v252
	v_med3_f32 v39, v39, s30, v252
	v_min_f32_e32 v28, 0x40e00000, v28
	v_min_f32_e32 v29, 0x40e00000, v29
	v_pk_mul_f32 v[42:43], v[30:31], s[86:87] op_sel_hi:[1,0]
	v_pk_fma_f32 v[30:31], v[30:31], v[38:39], v[30:31]
	v_pk_mul_f32 v[38:39], v[28:29], s[86:87] op_sel_hi:[1,0]
	v_pk_add_f32 v[36:37], v[168:169], v[10:11]
	v_exp_f32_e32 v38, v38
	v_exp_f32_e32 v39, v39
	v_med3_f32 v36, v36, s30, v252
	v_med3_f32 v37, v37, s30, v252
	v_min_f32_e32 v34, 0x40e00000, v34
	v_pk_add_f32 v[38:39], v[38:39], 1.0 op_sel_hi:[1,0]
	v_min_f32_e32 v35, 0x40e00000, v35
	v_rcp_f32_e32 v38, v38
	v_rcp_f32_e32 v39, v39
	v_pk_fma_f32 v[28:29], v[28:29], v[36:37], v[28:29]
	v_pk_mul_f32 v[36:37], v[34:35], s[86:87] op_sel_hi:[1,0]
	v_exp_f32_e32 v42, v42
	v_exp_f32_e32 v43, v43
	v_exp_f32_e32 v36, v36
	v_exp_f32_e32 v37, v37
	v_pk_add_f32 v[32:33], v[122:123], v[14:15]
	v_pk_add_f32 v[44:45], v[170:171], v[4:5]
	v_pk_mul_f32 v[28:29], v[28:29], v[38:39]
	v_med3_f32 v38, v44, s30, v252
	v_med3_f32 v39, v45, s30, v252
	v_min_f32_e32 v32, 0x40e00000, v32
	v_min_f32_e32 v33, 0x40e00000, v33
	v_pk_fma_f32 v[34:35], v[34:35], v[38:39], v[34:35]
	v_pk_mul_f32 v[38:39], v[32:33], s[86:87] op_sel_hi:[1,0]
	v_or_b32_e32 v26, 16, v24
	v_pk_add_f32 v[42:43], v[42:43], 1.0 op_sel_hi:[1,0]
	v_pk_add_f32 v[36:37], v[36:37], 1.0 op_sel_hi:[1,0]
	v_exp_f32_e32 v38, v38
	v_exp_f32_e32 v39, v39
	v_ashrrev_i32_e32 v27, 31, v26
	v_rcp_f32_e32 v42, v42
	v_rcp_f32_e32 v43, v43
	v_rcp_f32_e32 v36, v36
	v_rcp_f32_e32 v37, v37
	v_lshlrev_b64 v[26:27], 10, v[26:27]
	v_lshl_add_u64 v[26:27], v[22:23], 0, v[26:27]
	ds_bpermute_b32 v56, v46, v40
	ds_bpermute_b32 v57, v46, v41
	s_waitcnt lgkmcnt(2)
	global_store_dwordx2 v52, v[48:49], s[74:75]
	s_add_u32 s74, s74, 0x4000
	s_addc_u32 s75, s75, 0
	v_pk_add_f32 v[40:41], v[172:173], v[6:7]
	v_pk_add_f32 v[38:39], v[38:39], 1.0 op_sel_hi:[1,0]
	v_pk_mul_f32 v[30:31], v[30:31], v[42:43]
	v_pk_mul_f32 v[34:35], v[34:35], v[36:37]
	v_med3_f32 v36, v40, s30, v252
	v_med3_f32 v37, v41, s30, v252
	v_rcp_f32_e32 v38, v38
	v_rcp_f32_e32 v39, v39
	v_mov_b32_e32 v40, v3
	v_mov_b32_e32 v41, v3
	v_cvt_pk_fp8_f32 v40, v30, v31
	v_cvt_pk_fp8_f32 v41, v34, v35
	v_pk_fma_f32 v[30:31], v[32:33], v[36:37], v[32:33]
	v_or_b32_e32 v26, 32, v24
	v_pk_mul_f32 v[30:31], v[30:31], v[38:39]
	v_cvt_pk_fp8_f32 v40, v28, v29 op_sel:[0,0,1]
	v_cvt_pk_fp8_f32 v41, v30, v31 op_sel:[0,0,1]
	v_ashrrev_i32_e32 v27, 31, v26
	v_lshlrev_b64 v[26:27], 10, v[26:27]
	v_lshl_add_u64 v[26:27], v[22:23], 0, v[26:27]
	ds_bpermute_b32 v48, v46, v40
	ds_bpermute_b32 v49, v46, v41
	s_waitcnt lgkmcnt(2)
	global_store_dwordx2 v52, v[56:57], s[74:75]
	s_add_u32 s74, s74, 0x4000
	s_addc_u32 s75, s75, 0
	v_pk_add_f32 v[26:27], v[130:131], v[18:19]
	v_pk_add_f32 v[28:29], v[128:129], v[16:17]
	v_pk_add_f32 v[36:37], v[174:175], v[8:9]
	v_min_f32_e32 v28, 0x40e00000, v28
	v_min_f32_e32 v29, 0x40e00000, v29
	v_med3_f32 v36, v36, s30, v252
	v_med3_f32 v37, v37, s30, v252
	v_min_f32_e32 v26, 0x40e00000, v26
	v_min_f32_e32 v27, 0x40e00000, v27
	v_pk_mul_f32 v[40:41], v[28:29], s[86:87] op_sel_hi:[1,0]
	v_pk_fma_f32 v[28:29], v[28:29], v[36:37], v[28:29]
	v_pk_mul_f32 v[36:37], v[26:27], s[86:87] op_sel_hi:[1,0]
	v_pk_add_f32 v[32:33], v[132:133], v[12:13]
	v_exp_f32_e32 v36, v36
	v_exp_f32_e32 v37, v37
	v_pk_add_f32 v[34:35], v[176:177], v[10:11]
	v_min_f32_e32 v32, 0x40e00000, v32
	v_med3_f32 v34, v34, s30, v252
	v_pk_add_f32 v[36:37], v[36:37], 1.0 op_sel_hi:[1,0]
	v_med3_f32 v35, v35, s30, v252
	v_rcp_f32_e32 v36, v36
	v_rcp_f32_e32 v37, v37
	v_min_f32_e32 v33, 0x40e00000, v33
	v_pk_fma_f32 v[26:27], v[26:27], v[34:35], v[26:27]
	v_pk_mul_f32 v[34:35], v[32:33], s[86:87] op_sel_hi:[1,0]
	v_exp_f32_e32 v40, v40
	v_exp_f32_e32 v41, v41
	v_exp_f32_e32 v34, v34
	v_exp_f32_e32 v35, v35
	v_pk_add_f32 v[30:31], v[134:135], v[14:15]
	v_pk_add_f32 v[42:43], v[182:183], v[4:5]
	v_pk_mul_f32 v[26:27], v[26:27], v[36:37]
	v_med3_f32 v36, v42, s30, v252
	v_med3_f32 v37, v43, s30, v252
	v_min_f32_e32 v30, 0x40e00000, v30
	v_min_f32_e32 v31, 0x40e00000, v31
	v_pk_fma_f32 v[32:33], v[32:33], v[36:37], v[32:33]
	v_pk_mul_f32 v[36:37], v[30:31], s[86:87] op_sel_hi:[1,0]
	v_pk_add_f32 v[40:41], v[40:41], 1.0 op_sel_hi:[1,0]
	v_pk_add_f32 v[34:35], v[34:35], 1.0 op_sel_hi:[1,0]
	v_exp_f32_e32 v36, v36
	v_exp_f32_e32 v37, v37
	v_rcp_f32_e32 v40, v40
	v_rcp_f32_e32 v41, v41
	v_rcp_f32_e32 v34, v34
	v_rcp_f32_e32 v35, v35
	v_pk_add_f32 v[38:39], v[184:185], v[6:7]
	v_pk_add_f32 v[36:37], v[36:37], 1.0 op_sel_hi:[1,0]
	v_pk_mul_f32 v[28:29], v[28:29], v[40:41]
	v_pk_mul_f32 v[32:33], v[32:33], v[34:35]
	v_med3_f32 v34, v38, s30, v252
	v_med3_f32 v35, v39, s30, v252
	v_rcp_f32_e32 v36, v36
	v_rcp_f32_e32 v37, v37
	v_mov_b32_e32 v38, v3
	v_mov_b32_e32 v39, v3
	v_cvt_pk_fp8_f32 v38, v28, v29
	v_cvt_pk_fp8_f32 v39, v32, v33
	v_pk_fma_f32 v[28:29], v[30:31], v[34:35], v[30:31]
	v_or_b32_e32 v24, 48, v24
	v_pk_mul_f32 v[28:29], v[28:29], v[36:37]
	v_cvt_pk_fp8_f32 v38, v26, v27 op_sel:[0,0,1]
	v_cvt_pk_fp8_f32 v39, v28, v29 op_sel:[0,0,1]
	v_ashrrev_i32_e32 v25, 31, v24
	v_lshlrev_b64 v[24:25], 10, v[24:25]
	v_lshl_add_u64 v[22:23], v[22:23], 0, v[24:25]
	ds_bpermute_b32 v56, v46, v38
	ds_bpermute_b32 v57, v46, v39
	s_waitcnt lgkmcnt(2)
	global_store_dwordx2 v52, v[48:49], s[74:75]
	s_add_u32 s74, s74, 0x4000
	s_addc_u32 s75, s75, 0
	v_pk_add_f32 v[22:23], v[70:71], v[18:19]
	v_pk_add_f32 v[24:25], v[68:69], v[16:17]
	v_pk_add_f32 v[32:33], v[124:125], v[8:9]
	v_min_f32_e32 v24, 0x40e00000, v24
	v_min_f32_e32 v25, 0x40e00000, v25
	v_med3_f32 v32, v32, s30, v252
	v_med3_f32 v33, v33, s30, v252
	v_min_f32_e32 v22, 0x40e00000, v22
	v_min_f32_e32 v23, 0x40e00000, v23
	v_pk_mul_f32 v[36:37], v[24:25], s[86:87] op_sel_hi:[1,0]
	v_pk_fma_f32 v[24:25], v[24:25], v[32:33], v[24:25]
	v_pk_mul_f32 v[32:33], v[22:23], s[86:87] op_sel_hi:[1,0]
	v_pk_add_f32 v[28:29], v[72:73], v[12:13]
	v_exp_f32_e32 v32, v32
	v_exp_f32_e32 v33, v33
	v_pk_add_f32 v[30:31], v[126:127], v[10:11]
	v_min_f32_e32 v28, 0x40e00000, v28
	v_med3_f32 v30, v30, s30, v252
	v_pk_add_f32 v[32:33], v[32:33], 1.0 op_sel_hi:[1,0]
	v_med3_f32 v31, v31, s30, v252
	v_rcp_f32_e32 v32, v32
	v_rcp_f32_e32 v33, v33
	v_min_f32_e32 v29, 0x40e00000, v29
	v_pk_fma_f32 v[22:23], v[22:23], v[30:31], v[22:23]
	v_pk_mul_f32 v[30:31], v[28:29], s[86:87] op_sel_hi:[1,0]
	v_exp_f32_e32 v36, v36
	v_exp_f32_e32 v37, v37
	v_exp_f32_e32 v30, v30
	v_exp_f32_e32 v31, v31
	v_pk_add_f32 v[26:27], v[74:75], v[14:15]
	v_pk_add_f32 v[38:39], v[136:137], v[4:5]
	v_pk_mul_f32 v[22:23], v[22:23], v[32:33]
	v_med3_f32 v32, v38, s30, v252
	v_med3_f32 v33, v39, s30, v252
	v_min_f32_e32 v26, 0x40e00000, v26
	v_min_f32_e32 v27, 0x40e00000, v27
	v_pk_fma_f32 v[28:29], v[28:29], v[32:33], v[28:29]
	v_pk_mul_f32 v[32:33], v[26:27], s[86:87] op_sel_hi:[1,0]
	v_pk_add_f32 v[36:37], v[36:37], 1.0 op_sel_hi:[1,0]
	v_pk_add_f32 v[30:31], v[30:31], 1.0 op_sel_hi:[1,0]
	v_exp_f32_e32 v32, v32
	v_exp_f32_e32 v33, v33
	v_rcp_f32_e32 v36, v36
	v_rcp_f32_e32 v37, v37
	v_rcp_f32_e32 v30, v30
	v_rcp_f32_e32 v31, v31
	v_pk_add_f32 v[34:35], v[138:139], v[6:7]
	v_pk_add_f32 v[32:33], v[32:33], 1.0 op_sel_hi:[1,0]
	v_pk_mul_f32 v[24:25], v[24:25], v[36:37]
	v_pk_mul_f32 v[28:29], v[28:29], v[30:31]
	v_med3_f32 v30, v34, s30, v252
	v_med3_f32 v31, v35, s30, v252
	v_rcp_f32_e32 v32, v32
	v_rcp_f32_e32 v33, v33
	v_mov_b32_e32 v34, v3
	v_mov_b32_e32 v35, v3
	v_cvt_pk_fp8_f32 v34, v24, v25
	v_cvt_pk_fp8_f32 v35, v28, v29
	v_pk_fma_f32 v[24:25], v[26:27], v[30:31], v[26:27]
	s_mov_b32 s3, 0x20000
	v_pk_mul_f32 v[24:25], v[24:25], v[32:33]
	v_cvt_pk_fp8_f32 v34, v22, v23 op_sel:[0,0,1]
	v_cvt_pk_fp8_f32 v35, v24, v25 op_sel:[0,0,1]
	v_add_co_u32_e32 v22, vcc, s3, v20
	v_pk_add_f32 v[24:25], v[76:77], v[16:17]
	s_nop 0
	v_addc_co_u32_e32 v23, vcc, 0, v21, vcc
	ds_bpermute_b32 v48, v46, v34
	ds_bpermute_b32 v49, v46, v35
	s_waitcnt lgkmcnt(2)
	global_store_dwordx2 v52, v[56:57], s[74:75]
	s_add_u32 s74, s74, 0x14000
	s_addc_u32 s75, s75, 0
	v_pk_add_f32 v[22:23], v[78:79], v[18:19]
	v_pk_add_f32 v[32:33], v[140:141], v[8:9]
	v_min_f32_e32 v24, 0x40e00000, v24
	v_min_f32_e32 v25, 0x40e00000, v25
	v_med3_f32 v32, v32, s30, v252
	v_med3_f32 v33, v33, s30, v252
	v_min_f32_e32 v22, 0x40e00000, v22
	v_min_f32_e32 v23, 0x40e00000, v23
	v_pk_mul_f32 v[36:37], v[24:25], s[86:87] op_sel_hi:[1,0]
	v_pk_fma_f32 v[24:25], v[24:25], v[32:33], v[24:25]
	v_pk_mul_f32 v[32:33], v[22:23], s[86:87] op_sel_hi:[1,0]
	v_pk_add_f32 v[28:29], v[84:85], v[12:13]
	v_exp_f32_e32 v32, v32
	v_exp_f32_e32 v33, v33
	v_pk_add_f32 v[30:31], v[142:143], v[10:11]
	v_min_f32_e32 v28, 0x40e00000, v28
	v_med3_f32 v30, v30, s30, v252
	v_pk_add_f32 v[32:33], v[32:33], 1.0 op_sel_hi:[1,0]
	v_med3_f32 v31, v31, s30, v252
	v_rcp_f32_e32 v32, v32
	v_rcp_f32_e32 v33, v33
	v_min_f32_e32 v29, 0x40e00000, v29
	v_pk_fma_f32 v[22:23], v[22:23], v[30:31], v[22:23]
	v_pk_mul_f32 v[30:31], v[28:29], s[86:87] op_sel_hi:[1,0]
	v_exp_f32_e32 v36, v36
	v_exp_f32_e32 v37, v37
	v_exp_f32_e32 v30, v30
	v_exp_f32_e32 v31, v31
	v_pk_add_f32 v[26:27], v[86:87], v[14:15]
	v_pk_add_f32 v[38:39], v[150:151], v[4:5]
	v_pk_mul_f32 v[22:23], v[22:23], v[32:33]
	v_med3_f32 v32, v38, s30, v252
	v_med3_f32 v33, v39, s30, v252
	v_min_f32_e32 v26, 0x40e00000, v26
	v_min_f32_e32 v27, 0x40e00000, v27
	v_pk_fma_f32 v[28:29], v[28:29], v[32:33], v[28:29]
	v_pk_mul_f32 v[32:33], v[26:27], s[86:87] op_sel_hi:[1,0]
	v_pk_add_f32 v[36:37], v[36:37], 1.0 op_sel_hi:[1,0]
	v_pk_add_f32 v[30:31], v[30:31], 1.0 op_sel_hi:[1,0]
	v_exp_f32_e32 v32, v32
	v_exp_f32_e32 v33, v33
	v_rcp_f32_e32 v36, v36
	v_rcp_f32_e32 v37, v37
	v_rcp_f32_e32 v30, v30
	v_rcp_f32_e32 v31, v31
	v_pk_add_f32 v[34:35], v[152:153], v[6:7]
	v_pk_add_f32 v[32:33], v[32:33], 1.0 op_sel_hi:[1,0]
	v_pk_mul_f32 v[24:25], v[24:25], v[36:37]
	v_pk_mul_f32 v[28:29], v[28:29], v[30:31]
	v_med3_f32 v30, v34, s30, v252
	v_med3_f32 v31, v35, s30, v252
	v_rcp_f32_e32 v32, v32
	v_rcp_f32_e32 v33, v33
	v_mov_b32_e32 v34, v3
	v_mov_b32_e32 v35, v3
	v_cvt_pk_fp8_f32 v34, v24, v25
	v_cvt_pk_fp8_f32 v35, v28, v29
	v_pk_fma_f32 v[24:25], v[26:27], v[30:31], v[26:27]
	s_mov_b32 s3, 0x24000
	v_pk_mul_f32 v[24:25], v[24:25], v[32:33]
	v_cvt_pk_fp8_f32 v34, v22, v23 op_sel:[0,0,1]
	v_cvt_pk_fp8_f32 v35, v24, v25 op_sel:[0,0,1]
	v_add_co_u32_e32 v22, vcc, s3, v20
	v_pk_add_f32 v[24:25], v[92:93], v[16:17]
	s_nop 0
	v_addc_co_u32_e32 v23, vcc, 0, v21, vcc
	ds_bpermute_b32 v56, v46, v34
	ds_bpermute_b32 v57, v46, v35
	s_waitcnt lgkmcnt(2)
	global_store_dwordx2 v52, v[48:49], s[74:75]
	s_add_u32 s74, s74, 0x4000
	s_addc_u32 s75, s75, 0
	v_pk_add_f32 v[22:23], v[94:95], v[18:19]
	v_pk_add_f32 v[32:33], v[178:179], v[8:9]
	v_min_f32_e32 v24, 0x40e00000, v24
	v_min_f32_e32 v25, 0x40e00000, v25
	v_med3_f32 v32, v32, s30, v252
	v_med3_f32 v33, v33, s30, v252
	v_min_f32_e32 v22, 0x40e00000, v22
	v_min_f32_e32 v23, 0x40e00000, v23
	v_pk_mul_f32 v[36:37], v[24:25], s[86:87] op_sel_hi:[1,0]
	v_pk_fma_f32 v[24:25], v[24:25], v[32:33], v[24:25]
	v_pk_mul_f32 v[32:33], v[22:23], s[86:87] op_sel_hi:[1,0]
	v_pk_add_f32 v[28:29], v[100:101], v[12:13]
	v_exp_f32_e32 v32, v32
	v_exp_f32_e32 v33, v33
	v_pk_add_f32 v[30:31], v[180:181], v[10:11]
	v_min_f32_e32 v28, 0x40e00000, v28
	v_med3_f32 v30, v30, s30, v252
	v_pk_add_f32 v[32:33], v[32:33], 1.0 op_sel_hi:[1,0]
	v_med3_f32 v31, v31, s30, v252
	v_rcp_f32_e32 v32, v32
	v_rcp_f32_e32 v33, v33
	v_min_f32_e32 v29, 0x40e00000, v29
	v_pk_fma_f32 v[22:23], v[22:23], v[30:31], v[22:23]
	v_pk_mul_f32 v[30:31], v[28:29], s[86:87] op_sel_hi:[1,0]
	v_exp_f32_e32 v36, v36
	v_exp_f32_e32 v37, v37
	v_exp_f32_e32 v30, v30
	v_exp_f32_e32 v31, v31
	v_pk_add_f32 v[26:27], v[102:103], v[14:15]
	v_pk_add_f32 v[38:39], v[186:187], v[4:5]
	v_pk_mul_f32 v[22:23], v[22:23], v[32:33]
	v_med3_f32 v32, v38, s30, v252
	v_med3_f32 v33, v39, s30, v252
	v_min_f32_e32 v26, 0x40e00000, v26
	v_min_f32_e32 v27, 0x40e00000, v27
	v_pk_fma_f32 v[28:29], v[28:29], v[32:33], v[28:29]
	v_pk_mul_f32 v[32:33], v[26:27], s[86:87] op_sel_hi:[1,0]
	v_pk_add_f32 v[36:37], v[36:37], 1.0 op_sel_hi:[1,0]
	v_pk_add_f32 v[30:31], v[30:31], 1.0 op_sel_hi:[1,0]
	v_exp_f32_e32 v32, v32
	v_exp_f32_e32 v33, v33
	v_rcp_f32_e32 v36, v36
	v_rcp_f32_e32 v37, v37
	v_rcp_f32_e32 v30, v30
	v_rcp_f32_e32 v31, v31
	v_pk_add_f32 v[34:35], v[188:189], v[6:7]
	v_pk_add_f32 v[32:33], v[32:33], 1.0 op_sel_hi:[1,0]
	v_pk_mul_f32 v[24:25], v[24:25], v[36:37]
	v_pk_mul_f32 v[28:29], v[28:29], v[30:31]
	v_med3_f32 v30, v34, s30, v252
	v_med3_f32 v31, v35, s30, v252
	v_rcp_f32_e32 v32, v32
	v_rcp_f32_e32 v33, v33
	v_mov_b32_e32 v34, v3
	v_mov_b32_e32 v35, v3
	v_cvt_pk_fp8_f32 v34, v24, v25
	v_cvt_pk_fp8_f32 v35, v28, v29
	v_pk_fma_f32 v[24:25], v[26:27], v[30:31], v[26:27]
	s_mov_b32 s3, 0x28000
	v_pk_mul_f32 v[24:25], v[24:25], v[32:33]
	v_cvt_pk_fp8_f32 v34, v22, v23 op_sel:[0,0,1]
	v_cvt_pk_fp8_f32 v35, v24, v25 op_sel:[0,0,1]
	v_add_co_u32_e32 v22, vcc, s3, v20
	v_pk_add_f32 v[16:17], v[108:109], v[16:17]
	v_pk_add_f32 v[8:9], v[190:191], v[8:9]
	v_addc_co_u32_e32 v23, vcc, 0, v21, vcc
	v_pk_add_f32 v[18:19], v[110:111], v[18:19]
	v_pk_add_f32 v[12:13], v[116:117], v[12:13]
	v_pk_add_f32 v[10:11], v[192:193], v[10:11]
	v_min_f32_e32 v16, 0x40e00000, v16
	v_min_f32_e32 v17, 0x40e00000, v17
	v_med3_f32 v8, v8, s30, v252
	v_med3_f32 v9, v9, s30, v252
	ds_bpermute_b32 v48, v46, v34
	ds_bpermute_b32 v49, v46, v35
	s_waitcnt lgkmcnt(2)
	global_store_dwordx2 v52, v[56:57], s[74:75]
	s_add_u32 s74, s74, 0x4000
	s_addc_u32 s75, s75, 0
	v_pk_mul_f32 v[22:23], v[16:17], s[86:87] op_sel_hi:[1,0]
	v_pk_fma_f32 v[8:9], v[16:17], v[8:9], v[16:17]
	v_min_f32_e32 v16, 0x40e00000, v18
	v_min_f32_e32 v17, 0x40e00000, v19
	v_med3_f32 v10, v10, s30, v252
	v_med3_f32 v11, v11, s30, v252
	v_min_f32_e32 v12, 0x40e00000, v12
	v_min_f32_e32 v13, 0x40e00000, v13
	v_pk_mul_f32 v[18:19], v[16:17], s[86:87] op_sel_hi:[1,0]
	v_pk_fma_f32 v[10:11], v[16:17], v[10:11], v[16:17]
	v_pk_mul_f32 v[16:17], v[12:13], s[86:87] op_sel_hi:[1,0]
	v_exp_f32_e32 v22, v22
	v_exp_f32_e32 v23, v23
	v_pk_add_f32 v[4:5], v[194:195], v[4:5]
	v_exp_f32_e32 v16, v16
	v_exp_f32_e32 v17, v17
	v_pk_add_f32 v[14:15], v[118:119], v[14:15]
	v_med3_f32 v4, v4, s30, v252
	v_med3_f32 v5, v5, s30, v252
	v_pk_fma_f32 v[4:5], v[12:13], v[4:5], v[12:13]
	v_min_f32_e32 v12, 0x40e00000, v14
	v_min_f32_e32 v13, 0x40e00000, v15
	v_pk_mul_f32 v[14:15], v[12:13], s[86:87] op_sel_hi:[1,0]
	v_pk_add_f32 v[22:23], v[22:23], 1.0 op_sel_hi:[1,0]
	v_exp_f32_e32 v18, v18
	v_exp_f32_e32 v19, v19
	v_pk_add_f32 v[16:17], v[16:17], 1.0 op_sel_hi:[1,0]
	v_exp_f32_e32 v14, v14
	v_exp_f32_e32 v15, v15
	v_rcp_f32_e32 v22, v22
	v_rcp_f32_e32 v23, v23
	v_rcp_f32_e32 v16, v16
	v_rcp_f32_e32 v17, v17
	v_pk_add_f32 v[18:19], v[18:19], 1.0 op_sel_hi:[1,0]
	v_pk_add_f32 v[14:15], v[14:15], 1.0 op_sel_hi:[1,0]
	v_pk_mul_f32 v[8:9], v[8:9], v[22:23]
	v_rcp_f32_e32 v18, v18
	v_rcp_f32_e32 v19, v19
	v_pk_mul_f32 v[4:5], v[4:5], v[16:17]
	v_rcp_f32_e32 v14, v14
	v_rcp_f32_e32 v15, v15
	v_mov_b32_e32 v16, v3
	v_mov_b32_e32 v17, v3
	v_pk_add_f32 v[6:7], v[196:197], v[6:7]
	v_cvt_pk_fp8_f32 v16, v8, v9
	v_cvt_pk_fp8_f32 v17, v4, v5
	v_med3_f32 v6, v6, s30, v252
	v_med3_f32 v7, v7, s30, v252
	v_pk_fma_f32 v[4:5], v[12:13], v[6:7], v[12:13]
	v_pk_mul_f32 v[10:11], v[10:11], v[18:19]
	v_pk_mul_f32 v[4:5], v[4:5], v[14:15]
	v_cvt_pk_fp8_f32 v16, v10, v11 op_sel:[0,0,1]
	v_cvt_pk_fp8_f32 v17, v4, v5 op_sel:[0,0,1]
	v_add_co_u32_e32 v4, vcc, 0x2c000, v20
	s_cmp_eq_u32 s68, s65
	s_nop 0
	v_addc_co_u32_e32 v5, vcc, 0, v21, vcc
	s_mov_b64 s[40:41], -1
	ds_bpermute_b32 v56, v46, v16
	ds_bpermute_b32 v57, v46, v17
	s_waitcnt lgkmcnt(2)
	global_store_dwordx2 v52, v[48:49], s[74:75]
	s_waitcnt lgkmcnt(0)
	global_store_dwordx2 v52, v[56:57], s[46:47]
	s_cbranch_scc1 .LBB0_882
	s_andn2_b64 vcc, exec, s[8:9]
	s_cbranch_vccnz .LBB0_902
	s_ashr_i32 s40, s20, 3
	s_ashr_i32 s41, s40, 31
	s_lshl_b64 s[40:41], s[40:41], 13
	s_add_u32 s3, s52, s40
	s_addc_u32 s21, s53, s41
	s_lshl_b32 s27, s20, 9
	s_and_b32 s27, s27, 0xe00
	s_add_u32 s40, s3, s27
	s_addc_u32 s41, s21, 0
	s_lshl_b32 s3, s67, 10
	v_mov_b32_e32 v203, v3
	s_and_b32 s3, s3, 0x400
	v_lshl_add_u64 v[4:5], s[40:41], 0, v[202:203]
	v_mov_b32_e32 v205, v3
	s_add_i32 s3, s3, 0
	v_lshl_add_u64 v[4:5], v[4:5], 0, v[204:205]
	s_add_i32 m0, s3, 0x24000
	s_nop 0
	global_load_lds_dwordx4 v[4:5], off
